# speedup vs baseline: 1.1249x; 1.0181x over previous
.LBB2_6:
	s_or_b64 exec, exec, s[18:19]
	v_xor_b32_e32 v23, 32, v23
	s_add_i32 s38, 0, 0x1c000
	v_lshlrev_b32_e32 v23, 2, v23
	v_lshlrev_b32_e32 v199, 2, v25
	s_waitcnt vmcnt(4) lgkmcnt(0)
	s_barrier
	v_add3_u32 v23, s38, v23, v199
	ds_read_b32 v23, v23
	v_max_f32_e32 v24, v24, v24
	v_mul_f32_e32 v22, 0x3db8aa3b, v22
	v_mov_b32_e32 v164, 0
	v_mov_b32_e32 v165, 0
	s_waitcnt lgkmcnt(0)
	s_movk_i32 s45, 0x4000
	v_add3_u32 v250, s45, v184, v185
	v_add3_u32 v251, s45, v184, v186
	v_add3_u32 v252, s45, v184, v187
	v_add3_u32 v253, s45, v184, v188
	ds_read_b128 v[218:221], v250 offset:49152
	ds_read_b128 v[222:225], v251 offset:49152
	ds_read_b128 v[242:245], v252 offset:49152
	ds_read_b128 v[246:249], v253 offset:49152
	v_add3_u32 v250, s45, v184, v189
	v_add3_u32 v251, s45, v184, v190
	v_add3_u32 v252, s45, v184, v191
	v_add3_u32 v253, s45, v184, v192
	ds_read_b128 v[202:205], v250 offset:49152
	ds_read_b128 v[206:209], v251 offset:49152
	ds_read_b128 v[210:213], v252 offset:49152
	ds_read_b128 v[214:217], v253 offset:49152
	v_max_f32_e32 v23, v23, v23
	v_max_f32_e32 v197, v24, v23
	v_mov_b32_e32 v23, 2.0
	v_fmamk_f32 v200, v197, 0xbdb8aa3b, v23
	v_fmamk_f32 v23, v22, 0xcb400000, v200
	v_fma_f32 v2, v2, v22, v23
	v_fma_f32 v3, v3, v22, v23
	v_fma_f32 v6, v6, v22, v23
	v_fma_f32 v7, v7, v22, v23
	v_fma_f32 v10, v10, v22, v23
	v_fma_f32 v11, v11, v22, v23
	v_fma_f32 v14, v14, v22, v23
	v_fma_f32 v15, v15, v22, v23
	v_exp_f32_e32 v2, v2
	v_exp_f32_e32 v3, v3
	v_exp_f32_e32 v6, v6
	v_exp_f32_e32 v7, v7
	v_exp_f32_e32 v10, v10
	v_exp_f32_e32 v11, v11
	v_exp_f32_e32 v14, v14
	v_exp_f32_e32 v15, v15
	v_fma_f32 v4, v4, v22, v23
	v_fma_f32 v5, v5, v22, v23
	v_fma_f32 v8, v8, v22, v23
	v_fma_f32 v9, v9, v22, v23
	v_fma_f32 v12, v12, v22, v23
	v_fma_f32 v13, v13, v22, v23
	v_fma_f32 v16, v16, v22, v23
	v_fmac_f32_e32 v23, v17, v22
	v_mov_b32_e32 v166, 0
	v_mov_b32_e32 v167, 0
	v_exp_f32_e32 v4, v4
	v_exp_f32_e32 v5, v5
	v_exp_f32_e32 v8, v8
	v_exp_f32_e32 v9, v9
	v_exp_f32_e32 v12, v12
	v_exp_f32_e32 v13, v13
	v_exp_f32_e32 v16, v16
	v_exp_f32_e32 v17, v23
	v_add_f32_e32 v250, v2, v3
	v_add_f32_e32 v251, v4, v5
	v_add_f32_e32 v252, v6, v7
	v_add_f32_e32 v253, v8, v9
	v_add_f32_e32 v250, v250, v251
	v_add_f32_e32 v252, v252, v253
	v_add_f32_e32 v251, v10, v11
	v_add_f32_e32 v253, v12, v13
	v_add_f32_e32 v250, v250, v252
	v_add_f32_e32 v251, v251, v253
	v_add_f32_e32 v252, v14, v15
	v_add_f32_e32 v253, v16, v17
	v_add_f32_e32 v250, v250, v251
	v_add_f32_e32 v252, v252, v253
	v_add_f32_e32 v250, v250, v252
	v_cvt_pk_fp8_f32 v164, v2, v3
	v_cvt_pk_fp8_f32 v165, v6, v7
	v_cvt_pk_fp8_f32 v166, v10, v11
	v_cvt_pk_fp8_f32 v167, v14, v15
	s_lshl_b32 s0, s22, 11
	s_add_i32 s0, s0, 0
	s_add_i32 s0, s0, 0x18000
	v_cvt_pk_fp8_f32 v164, v4, v5 op_sel:[0,0,1]
	v_cvt_pk_fp8_f32 v165, v8, v9 op_sel:[0,0,1]
	v_cvt_pk_fp8_f32 v166, v12, v13 op_sel:[0,0,1]
	v_cvt_pk_fp8_f32 v167, v16, v17 op_sel:[0,0,1]
	v_lshl_add_u32 v193, v198, 5, s0
	v_lshrrev_b32_e32 v3, 2, v0
	v_lshlrev_b32_e32 v6, 1, v183
	s_lshl_b32 s0, s20, 20
	v_bfe_u32 v4, v0, 2, 2
	v_lshl_or_b32 v5, v1, 6, s24
	v_bitop3_b32 v3, v6, v3, 3 bitop3:0x78
	s_or_b32 s18, s0, s23
	v_lshl_add_u32 v194, s34, 4, v193
	v_lshl_or_b32 v195, v3, 4, v5
	v_bitop3_b32 v3, v6, v4, 1 bitop3:0x36
	v_add3_u32 v4, s21, v20, v21
	s_add_u32 s0, s6, s18
	ds_write_b128 v194, v[164:167]
	v_lshl_or_b32 v196, v3, 4, v5
	v_ashrrev_i32_e32 v5, 31, v4
	s_addc_u32 s1, s7, 0
	s_waitcnt vmcnt(2) lgkmcnt(0)
	s_barrier
	s_mov_b64 s[60:61], s[0:1]
	v_lshl_add_u64 v[170:171], s[0:1], 0, v[4:5]
	v_add3_u32 v4, s21, v18, v19
	s_add_u32 s0, s8, s18
	v_mov_b32_e32 v2, 0
	v_ashrrev_i32_e32 v5, 31, v4
	s_addc_u32 s1, s9, 0
	s_mov_b32 s39, 0
	s_mov_b32 s40, 1
	s_mov_b64 s[64:65], s[0:1]
	v_lshl_add_u64 v[172:173], s[0:1], 0, v[4:5]
	s_mov_b64 s[6:7], 0
	s_movk_i32 s41, 0x2000
	s_mov_b64 s[8:9], 0xc000
	s_mov_b64 s[18:19], 0xe000
	s_mov_b64 s[20:21], 0x8000
	s_mov_b64 s[22:23], 0xa000
	s_mov_b32 s42, 0x42966666
	v_mov_b32_e32 v82, 0x4b400000
	v_mov_b32_e32 v100, 0x38383838
	s_mov_b32 s0, 0
	s_mov_b32 s43, 1
	v_mov_b32_e32 v3, v2
	v_mov_b32_e32 v4, v2
	v_mov_b32_e32 v5, v2
	v_mov_b32_e32 v6, v2
	v_mov_b32_e32 v7, v2
	v_mov_b32_e32 v8, v2
	v_mov_b32_e32 v9, v2
	v_mov_b32_e32 v10, v2
	v_mov_b32_e32 v11, v2
	v_mov_b32_e32 v12, v2
	v_mov_b32_e32 v13, v2
	v_mov_b32_e32 v14, v2
	v_mov_b32_e32 v15, v2
	v_mov_b32_e32 v16, v2
	v_mov_b32_e32 v17, v2
	v_mov_b32_e32 v18, v2
	v_mov_b32_e32 v19, v2
	v_mov_b32_e32 v20, v2
	v_mov_b32_e32 v21, v2
	v_mov_b32_e32 v22, v2
	v_mov_b32_e32 v23, v2
	v_mov_b32_e32 v24, v2
	v_mov_b32_e32 v25, v2
	v_mov_b32_e32 v26, v2
	v_mov_b32_e32 v27, v2
	v_mov_b32_e32 v28, v2
	v_mov_b32_e32 v29, v2
	v_mov_b32_e32 v30, v2
	v_mov_b32_e32 v31, v2
	v_mov_b32_e32 v32, v2
	v_mov_b32_e32 v33, v2
	v_mov_b32_e32 v34, v2
	v_mov_b32_e32 v35, v2
	v_mov_b32_e32 v36, v2
	v_mov_b32_e32 v37, v2
	v_mov_b32_e32 v38, v2
	v_mov_b32_e32 v39, v2
	v_mov_b32_e32 v40, v2
	v_mov_b32_e32 v41, v2
	v_mov_b32_e32 v42, v2
	v_mov_b32_e32 v43, v2
	v_mov_b32_e32 v44, v2
	v_mov_b32_e32 v45, v2
	v_mov_b32_e32 v46, v2
	v_mov_b32_e32 v47, v2
	v_mov_b32_e32 v48, v2
	v_mov_b32_e32 v49, v2
	v_mov_b32_e32 v50, v2
	v_mov_b32_e32 v51, v2
	v_mov_b32_e32 v52, v2
	v_mov_b32_e32 v53, v2
	v_mov_b32_e32 v54, v2
	v_mov_b32_e32 v55, v2
	v_mov_b32_e32 v56, v2
	v_mov_b32_e32 v57, v2
	v_mov_b32_e32 v58, v2
	v_mov_b32_e32 v59, v2
	v_mov_b32_e32 v60, v2
	v_mov_b32_e32 v61, v2
	v_mov_b32_e32 v62, v2
	v_mov_b32_e32 v63, v2
	v_mov_b32_e32 v64, v2
	v_mov_b32_e32 v65, v2
	v_mov_b32_e32 v66, v2
	v_mov_b32_e32 v67, v2
	v_mov_b32_e32 v68, v2
	v_mov_b32_e32 v69, v2
	v_mov_b32_e32 v70, v2
	v_mov_b32_e32 v71, v2
	v_mov_b32_e32 v72, v2
	v_mov_b32_e32 v73, v2
	v_mov_b32_e32 v74, v2
	v_mov_b32_e32 v75, v2
	v_mov_b32_e32 v76, v2
	v_mov_b32_e32 v77, v2
	v_mov_b32_e32 v78, v2
	v_mov_b32_e32 v79, v2
	v_mov_b32_e32 v80, v2
	v_mov_b32_e32 v81, v2
	v_mov_b32_e32 v66, v250
	v_mov_b32_e32 v226, 0x4b400000
	v_mov_b32_e32 v227, v226
	v_mov_b32_e32 v228, v226
	v_mov_b32_e32 v229, v226
	v_mov_b32_e32 v230, v226
	v_mov_b32_e32 v231, v226
	v_mov_b32_e32 v232, v226
	v_mov_b32_e32 v233, v226
	v_mov_b32_e32 v234, v226
	v_mov_b32_e32 v235, v226
	v_mov_b32_e32 v236, v226
	v_mov_b32_e32 v237, v226
	v_mov_b32_e32 v238, v226
	v_mov_b32_e32 v239, v226
	v_mov_b32_e32 v240, v226
	v_mov_b32_e32 v241, v226
	v_add_u32_e32 v250, 0xc000, v184
	v_add_u32_e32 v185, v185, v250
	v_add_u32_e32 v186, v186, v250
	v_add_u32_e32 v187, v187, v250
	v_add_u32_e32 v188, v188, v250
	v_add_u32_e32 v189, v189, v250
	v_add_u32_e32 v190, v190, v250
	v_add_u32_e32 v191, v191, v250
	v_add_u32_e32 v192, v192, v250
	v_subrev_u32_e32 v252, s60, v170
	v_subrev_u32_e32 v255, s64, v172
	s_sub_u32 s1, s64, s60
	s_add_i32 s1, s1, 0xffffc000
	v_add_u32_e32 v254, 0x2000, v252
	v_add_u32_e32 v255, s1, v255
	v_add_u32_e32 v201, 0x2000, v255
	s_add_u32 s60, s60, 0xc000
	s_addc_u32 s61, s61, 0
	s_mov_b32 s42, 0x43dc0000
	s_mov_b64 s[54:55], -1
	v_mfma_i32_32x32x32_i8 v[84:99], v[218:221], v[132:135], v[226:241]
	v_mfma_i32_32x32x32_i8 v[84:99], v[222:225], v[136:139], v[84:99]

.Lat_k0:
	ds_read_b128 v[128:131], v196 offset:4096
	v_mfma_i32_32x32x32_i8 v[84:99], v[202:205], v[148:151], v[84:99]
	ds_read_b128 v[202:205], v195
	v_mfma_i32_32x32x32_i8 v[84:99], v[206:209], v[152:155], v[84:99]
	ds_read_b128 v[206:209], v196
	v_mfma_i32_32x32x32_i8 v[84:99], v[210:213], v[156:159], v[84:99]
	ds_read_b128 v[210:213], v195 offset:2048
	v_mfma_i32_32x32x32_i8 v[84:99], v[214:217], v[160:163], v[84:99]
	ds_read_b128 v[214:217], v196 offset:2048
	v_readlane_b32 s50, v182, s43
	s_waitcnt lgkmcnt(6)
	v_mfma_f32_32x32x64_f8f6f4 v[2:17], v[108:115], v[116:123], v[2:17]
	ds_read_b128 v[218:221], v185 offset:32768
	ds_read_b128 v[222:225], v186 offset:32768
	ds_read_b128 v[242:245], v187 offset:32768
	ds_read_b128 v[246:249], v188 offset:32768
	v_mul_f32_e32 v82, s50, v168
	v_mul_f32_e32 v250, 0x3db8aa3b, v82
	v_fmamk_f32 v251, v250, 0xcb400000, v200
	s_cmp_gt_u32 s43, 30
	s_cbranch_scc1 .Lat_nov0
	s_add_i32 m0, s31, 32768
	v_fma_f32 v84, v84, v250, v251
	global_load_lds_dwordx4 v255, s[60:61]
	s_add_i32 m0, s31, 40960
	v_fma_f32 v85, v85, v250, v251
	global_load_lds_dwordx4 v201, s[60:61]
	s_branch .Lat_v0
.Lat_nov0:
	v_fma_f32 v84, v84, v250, v251
	v_fma_f32 v85, v85, v250, v251
.Lat_v0:
	v_fma_f32 v86, v86, v250, v251
	v_fma_f32 v87, v87, v250, v251
	v_exp_f32_e32 v84, v84
	v_exp_f32_e32 v85, v85
	v_exp_f32_e32 v86, v86
	v_exp_f32_e32 v87, v87
	v_fma_f32 v88, v88, v250, v251
	v_fma_f32 v89, v89, v250, v251
	v_fma_f32 v90, v90, v250, v251
	v_fma_f32 v91, v91, v250, v251
	s_waitcnt lgkmcnt(8)
	v_mfma_f32_32x32x64_f8f6f4 v[18:33], v[108:115], v[124:131], v[18:33]
	v_add_f32_e32 v67, v84, v85
	v_add_f32_e32 v68, v86, v87
	v_exp_f32_e32 v88, v88
	v_exp_f32_e32 v89, v89
	v_exp_f32_e32 v90, v90
	v_exp_f32_e32 v91, v91
	v_add_f32_e32 v67, v67, v68
	v_cvt_pk_fp8_f32 v164, v84, v85
	v_cvt_pk_fp8_f32 v164, v86, v87 op_sel:[0,0,1]
	v_fma_f32 v92, v92, v250, v251
	v_fma_f32 v93, v93, v250, v251
	v_fma_f32 v94, v94, v250, v251
	v_fma_f32 v95, v95, v250, v251
	v_add_f32_e32 v68, v88, v89
	v_add_f32_e32 v69, v90, v91
	s_waitcnt lgkmcnt(6)
	v_mfma_f32_32x32x64_f8f6f4 v[50:65], v[108:115], v[202:209], v[50:65]
	ds_read_b128 v[202:205], v189 offset:32768
	ds_read_b128 v[206:209], v190 offset:32768
	v_exp_f32_e32 v92, v92
	v_exp_f32_e32 v93, v93
	v_exp_f32_e32 v94, v94
	v_exp_f32_e32 v95, v95
	v_add_f32_e32 v68, v68, v69
	v_cvt_pk_fp8_f32 v165, v88, v89
	v_cvt_pk_fp8_f32 v165, v90, v91 op_sel:[0,0,1]
	v_fma_f32 v96, v96, v250, v251
	v_fma_f32 v97, v97, v250, v251
	v_fma_f32 v98, v98, v250, v251
	v_fma_f32 v99, v99, v250, v251
	v_add_f32_e32 v67, v67, v68
	v_add_f32_e32 v68, v92, v93
	v_add_f32_e32 v69, v94, v95
	s_waitcnt lgkmcnt(6)
	v_mfma_f32_32x32x64_f8f6f4 v[34:49], v[108:115], v[210:217], v[34:49]
	ds_read_b128 v[210:213], v191 offset:32768
	ds_read_b128 v[214:217], v192 offset:32768
	v_exp_f32_e32 v96, v96
	v_exp_f32_e32 v97, v97
	v_exp_f32_e32 v98, v98
	v_exp_f32_e32 v99, v99
	v_add_f32_e32 v68, v68, v69
	v_cvt_pk_fp8_f32 v166, v92, v93
	v_cvt_pk_fp8_f32 v166, v94, v95 op_sel:[0,0,1]
	v_add_f32_e32 v67, v67, v68
	v_add_f32_e32 v68, v96, v97
	v_add_f32_e32 v69, v98, v99
	s_add_u32 s60, s60, 0x4000
	s_addc_u32 s61, s61, 0
	v_add_f32_e32 v68, v68, v69
	v_cvt_pk_fp8_f32 v167, v96, v97
	v_cvt_pk_fp8_f32 v167, v98, v99 op_sel:[0,0,1]
	v_add_f32_e32 v67, v67, v68
	ds_write_b128 v194, v[164:167] offset:8192
	v_cmp_ge_f32_e64 s[52:53], s42, v67
	v_add_f32_e32 v66, v66, v67
	s_add_i32 s43, s43, 1
	s_nop 0
	s_and_b64 s[54:55], s[54:55], s[52:53]
	s_cmp_eq_u32 s43, 32
	s_cbranch_scc1 .Lat_last
	s_waitcnt lgkmcnt(7)
	v_mfma_i32_32x32x32_i8 v[84:99], v[218:221], v[132:135], v[226:241]
	v_mfma_i32_32x32x32_i8 v[84:99], v[222:225], v[136:139], v[84:99]
	s_waitcnt vmcnt(2) lgkmcnt(0)
	s_barrier
.Lat_u1:
	ds_read_b128 v[108:111], v193 offset:8192
	ds_read_b128 v[112:115], v193 offset:8208
	v_mfma_i32_32x32x32_i8 v[84:99], v[242:245], v[140:143], v[84:99]
	ds_read_b128 v[116:119], v195 offset:22528
	ds_read_b128 v[120:123], v196 offset:22528
	s_add_i32 m0, s31, 65536
	ds_read_b128 v[124:127], v195 offset:20480
	global_load_lds_dwordx4 v252, s[60:61]
	s_add_i32 m0, s31, 73728
	v_mfma_i32_32x32x32_i8 v[84:99], v[246:249], v[144:147], v[84:99]
	global_load_lds_dwordx4 v254, s[60:61]
	ds_read_b128 v[128:131], v196 offset:20480
	v_mfma_i32_32x32x32_i8 v[84:99], v[202:205], v[148:151], v[84:99]
	ds_read_b128 v[202:205], v195 offset:16384
	v_mfma_i32_32x32x32_i8 v[84:99], v[206:209], v[152:155], v[84:99]
	ds_read_b128 v[206:209], v196 offset:16384
	v_mfma_i32_32x32x32_i8 v[84:99], v[210:213], v[156:159], v[84:99]
	ds_read_b128 v[210:213], v195 offset:18432
	v_mfma_i32_32x32x32_i8 v[84:99], v[214:217], v[160:163], v[84:99]
	ds_read_b128 v[214:217], v196 offset:18432
	v_readlane_b32 s50, v182, s43
	s_waitcnt lgkmcnt(6)
	v_mfma_f32_32x32x64_f8f6f4 v[2:17], v[108:115], v[116:123], v[2:17]
	ds_read_b128 v[218:221], v185
	ds_read_b128 v[222:225], v186
	ds_read_b128 v[242:245], v187
	ds_read_b128 v[246:249], v188
	v_mul_f32_e32 v82, s50, v168
	v_mul_f32_e32 v250, 0x3db8aa3b, v82
	v_fmamk_f32 v251, v250, 0xcb400000, v200
	s_mov_b32 m0, s31
	v_fma_f32 v84, v84, v250, v251
	global_load_lds_dwordx4 v255, s[60:61]
	s_add_i32 m0, s31, 8192
	v_fma_f32 v85, v85, v250, v251
	global_load_lds_dwordx4 v201, s[60:61]
	v_fma_f32 v86, v86, v250, v251
	v_fma_f32 v87, v87, v250, v251
	v_exp_f32_e32 v84, v84
	v_exp_f32_e32 v85, v85
	v_exp_f32_e32 v86, v86
	v_exp_f32_e32 v87, v87
	v_fma_f32 v88, v88, v250, v251
	v_fma_f32 v89, v89, v250, v251
	v_fma_f32 v90, v90, v250, v251
	v_fma_f32 v91, v91, v250, v251
	s_waitcnt lgkmcnt(8)
	v_mfma_f32_32x32x64_f8f6f4 v[18:33], v[108:115], v[124:131], v[18:33]
	v_add_f32_e32 v67, v84, v85
	v_add_f32_e32 v68, v86, v87
	v_exp_f32_e32 v88, v88
	v_exp_f32_e32 v89, v89
	v_exp_f32_e32 v90, v90
	v_exp_f32_e32 v91, v91
	v_add_f32_e32 v67, v67, v68
	v_cvt_pk_fp8_f32 v164, v84, v85
	v_cvt_pk_fp8_f32 v164, v86, v87 op_sel:[0,0,1]
	v_fma_f32 v92, v92, v250, v251
	v_fma_f32 v93, v93, v250, v251
	v_fma_f32 v94, v94, v250, v251
	v_fma_f32 v95, v95, v250, v251
	v_add_f32_e32 v68, v88, v89
	v_add_f32_e32 v69, v90, v91
	s_waitcnt lgkmcnt(6)
	v_mfma_f32_32x32x64_f8f6f4 v[50:65], v[108:115], v[202:209], v[50:65]
	ds_read_b128 v[202:205], v189
	ds_read_b128 v[206:209], v190
	v_exp_f32_e32 v92, v92
	v_exp_f32_e32 v93, v93
	v_exp_f32_e32 v94, v94
	v_exp_f32_e32 v95, v95
	v_add_f32_e32 v68, v68, v69
	v_cvt_pk_fp8_f32 v165, v88, v89
	v_cvt_pk_fp8_f32 v165, v90, v91 op_sel:[0,0,1]
	v_fma_f32 v96, v96, v250, v251
	v_fma_f32 v97, v97, v250, v251
	v_fma_f32 v98, v98, v250, v251
	v_fma_f32 v99, v99, v250, v251
	v_add_f32_e32 v67, v67, v68
	v_add_f32_e32 v68, v92, v93
	v_add_f32_e32 v69, v94, v95
	s_waitcnt lgkmcnt(6)
	v_mfma_f32_32x32x64_f8f6f4 v[34:49], v[108:115], v[210:217], v[34:49]
	ds_read_b128 v[210:213], v191
	ds_read_b128 v[214:217], v192
	v_exp_f32_e32 v96, v96
	v_exp_f32_e32 v97, v97
	v_exp_f32_e32 v98, v98
	v_exp_f32_e32 v99, v99
	v_add_f32_e32 v68, v68, v69
	v_cvt_pk_fp8_f32 v166, v92, v93
	v_cvt_pk_fp8_f32 v166, v94, v95 op_sel:[0,0,1]
	v_add_f32_e32 v67, v67, v68
	v_add_f32_e32 v68, v96, v97
	v_add_f32_e32 v69, v98, v99
	s_add_u32 s60, s60, 0x4000
	s_addc_u32 s61, s61, 0
	v_add_f32_e32 v68, v68, v69
	v_cvt_pk_fp8_f32 v167, v96, v97
	v_cvt_pk_fp8_f32 v167, v98, v99 op_sel:[0,0,1]
	v_add_f32_e32 v67, v67, v68
	ds_write_b128 v194, v[164:167]
	v_cmp_ge_f32_e64 s[52:53], s42, v67
	v_add_f32_e32 v66, v66, v67
	s_add_i32 s43, s43, 1
	s_nop 0
	s_and_b64 s[54:55], s[54:55], s[52:53]
	s_waitcnt lgkmcnt(7)
	v_mfma_i32_32x32x32_i8 v[84:99], v[218:221], v[132:135], v[226:241]
	v_mfma_i32_32x32x32_i8 v[84:99], v[222:225], v[136:139], v[84:99]
	s_waitcnt vmcnt(2) lgkmcnt(0)
	s_barrier
.Lat_u2:
	ds_read_b128 v[108:111], v193
	ds_read_b128 v[112:115], v193 offset:16
	v_mfma_i32_32x32x32_i8 v[84:99], v[242:245], v[140:143], v[84:99]
	ds_read_b128 v[116:119], v195 offset:38912
	ds_read_b128 v[120:123], v196 offset:38912
	s_add_i32 m0, s31, 81920
	ds_read_b128 v[124:127], v195 offset:36864
	global_load_lds_dwordx4 v252, s[60:61]
	s_add_i32 m0, s31, 90112
	v_mfma_i32_32x32x32_i8 v[84:99], v[246:249], v[144:147], v[84:99]
	global_load_lds_dwordx4 v254, s[60:61]
	ds_read_b128 v[128:131], v196 offset:36864
	v_mfma_i32_32x32x32_i8 v[84:99], v[202:205], v[148:151], v[84:99]
	ds_read_b128 v[202:205], v195 offset:32768
	v_mfma_i32_32x32x32_i8 v[84:99], v[206:209], v[152:155], v[84:99]
	ds_read_b128 v[206:209], v196 offset:32768
	v_mfma_i32_32x32x32_i8 v[84:99], v[210:213], v[156:159], v[84:99]
	ds_read_b128 v[210:213], v195 offset:34816
	v_mfma_i32_32x32x32_i8 v[84:99], v[214:217], v[160:163], v[84:99]
	ds_read_b128 v[214:217], v196 offset:34816
	v_readlane_b32 s50, v182, s43
	s_waitcnt lgkmcnt(6)
	v_mfma_f32_32x32x64_f8f6f4 v[2:17], v[108:115], v[116:123], v[2:17]
	ds_read_b128 v[218:221], v185 offset:16384
	ds_read_b128 v[222:225], v186 offset:16384
	ds_read_b128 v[242:245], v187 offset:16384
	ds_read_b128 v[246:249], v188 offset:16384
	v_mul_f32_e32 v82, s50, v168
	v_mul_f32_e32 v250, 0x3db8aa3b, v82
	v_fmamk_f32 v251, v250, 0xcb400000, v200
	s_add_i32 m0, s31, 16384
	v_fma_f32 v84, v84, v250, v251
	global_load_lds_dwordx4 v255, s[60:61]
	s_add_i32 m0, s31, 24576
	v_fma_f32 v85, v85, v250, v251
	global_load_lds_dwordx4 v201, s[60:61]
	v_fma_f32 v86, v86, v250, v251
	v_fma_f32 v87, v87, v250, v251
	v_exp_f32_e32 v84, v84
	v_exp_f32_e32 v85, v85
	v_exp_f32_e32 v86, v86
	v_exp_f32_e32 v87, v87
	v_fma_f32 v88, v88, v250, v251
	v_fma_f32 v89, v89, v250, v251
	v_fma_f32 v90, v90, v250, v251
	v_fma_f32 v91, v91, v250, v251
	s_waitcnt lgkmcnt(8)
	v_mfma_f32_32x32x64_f8f6f4 v[18:33], v[108:115], v[124:131], v[18:33]
	v_add_f32_e32 v67, v84, v85
	v_add_f32_e32 v68, v86, v87
	v_exp_f32_e32 v88, v88
	v_exp_f32_e32 v89, v89
	v_exp_f32_e32 v90, v90
	v_exp_f32_e32 v91, v91
	v_add_f32_e32 v67, v67, v68
	v_cvt_pk_fp8_f32 v164, v84, v85
	v_cvt_pk_fp8_f32 v164, v86, v87 op_sel:[0,0,1]
	v_fma_f32 v92, v92, v250, v251
	v_fma_f32 v93, v93, v250, v251
	v_fma_f32 v94, v94, v250, v251
	v_fma_f32 v95, v95, v250, v251
	v_add_f32_e32 v68, v88, v89
	v_add_f32_e32 v69, v90, v91
	s_waitcnt lgkmcnt(6)
	v_mfma_f32_32x32x64_f8f6f4 v[50:65], v[108:115], v[202:209], v[50:65]
	ds_read_b128 v[202:205], v189 offset:16384
	ds_read_b128 v[206:209], v190 offset:16384
	v_exp_f32_e32 v92, v92
	v_exp_f32_e32 v93, v93
	v_exp_f32_e32 v94, v94
	v_exp_f32_e32 v95, v95
	v_add_f32_e32 v68, v68, v69
	v_cvt_pk_fp8_f32 v165, v88, v89
	v_cvt_pk_fp8_f32 v165, v90, v91 op_sel:[0,0,1]
	v_fma_f32 v96, v96, v250, v251
	v_fma_f32 v97, v97, v250, v251
	v_fma_f32 v98, v98, v250, v251
	v_fma_f32 v99, v99, v250, v251
	v_add_f32_e32 v67, v67, v68
	v_add_f32_e32 v68, v92, v93
	v_add_f32_e32 v69, v94, v95
	s_waitcnt lgkmcnt(6)
	v_mfma_f32_32x32x64_f8f6f4 v[34:49], v[108:115], v[210:217], v[34:49]
	ds_read_b128 v[210:213], v191 offset:16384
	ds_read_b128 v[214:217], v192 offset:16384
	v_exp_f32_e32 v96, v96
	v_exp_f32_e32 v97, v97
	v_exp_f32_e32 v98, v98
	v_exp_f32_e32 v99, v99
	v_add_f32_e32 v68, v68, v69
	v_cvt_pk_fp8_f32 v166, v92, v93
	v_cvt_pk_fp8_f32 v166, v94, v95 op_sel:[0,0,1]
	v_add_f32_e32 v67, v67, v68
	v_add_f32_e32 v68, v96, v97
	v_add_f32_e32 v69, v98, v99
	s_add_u32 s60, s60, 0x4000
	s_addc_u32 s61, s61, 0
	v_add_f32_e32 v68, v68, v69
	v_cvt_pk_fp8_f32 v167, v96, v97
	v_cvt_pk_fp8_f32 v167, v98, v99 op_sel:[0,0,1]
	v_add_f32_e32 v67, v67, v68
	ds_write_b128 v194, v[164:167] offset:8192
	v_cmp_ge_f32_e64 s[52:53], s42, v67
	v_add_f32_e32 v66, v66, v67
	s_add_i32 s43, s43, 1
	s_nop 0
	s_and_b64 s[54:55], s[54:55], s[52:53]
	s_waitcnt lgkmcnt(7)
	v_mfma_i32_32x32x32_i8 v[84:99], v[218:221], v[132:135], v[226:241]
	v_mfma_i32_32x32x32_i8 v[84:99], v[222:225], v[136:139], v[84:99]
	s_waitcnt vmcnt(2) lgkmcnt(0)
	s_barrier
.Lat_u3:
	ds_read_b128 v[108:111], v193 offset:8192
	ds_read_b128 v[112:115], v193 offset:8208
	v_mfma_i32_32x32x32_i8 v[84:99], v[242:245], v[140:143], v[84:99]
	ds_read_b128 v[116:119], v195 offset:6144
	ds_read_b128 v[120:123], v196 offset:6144
	s_add_i32 m0, s31, 49152
	ds_read_b128 v[124:127], v195 offset:4096
	global_load_lds_dwordx4 v252, s[60:61]
	s_add_i32 m0, s31, 57344
	v_mfma_i32_32x32x32_i8 v[84:99], v[246:249], v[144:147], v[84:99]
	global_load_lds_dwordx4 v254, s[60:61]
	ds_read_b128 v[128:131], v196 offset:4096
	v_mfma_i32_32x32x32_i8 v[84:99], v[202:205], v[148:151], v[84:99]
	ds_read_b128 v[202:205], v195
	v_mfma_i32_32x32x32_i8 v[84:99], v[206:209], v[152:155], v[84:99]
	ds_read_b128 v[206:209], v196
	v_mfma_i32_32x32x32_i8 v[84:99], v[210:213], v[156:159], v[84:99]
	ds_read_b128 v[210:213], v195 offset:2048
	v_mfma_i32_32x32x32_i8 v[84:99], v[214:217], v[160:163], v[84:99]
	ds_read_b128 v[214:217], v196 offset:2048
	v_readlane_b32 s50, v182, s43
	s_waitcnt lgkmcnt(6)
	v_mfma_f32_32x32x64_f8f6f4 v[2:17], v[108:115], v[116:123], v[2:17]
	ds_read_b128 v[218:221], v185 offset:32768
	ds_read_b128 v[222:225], v186 offset:32768
	ds_read_b128 v[242:245], v187 offset:32768
	ds_read_b128 v[246:249], v188 offset:32768
	v_mul_f32_e32 v82, s50, v168
	v_mul_f32_e32 v250, 0x3db8aa3b, v82
	v_fmamk_f32 v251, v250, 0xcb400000, v200
	s_add_i32 m0, s31, 32768
	v_fma_f32 v84, v84, v250, v251
	global_load_lds_dwordx4 v255, s[60:61]
	s_add_i32 m0, s31, 40960
	v_fma_f32 v85, v85, v250, v251
	global_load_lds_dwordx4 v201, s[60:61]
	v_fma_f32 v86, v86, v250, v251
	v_fma_f32 v87, v87, v250, v251
	v_exp_f32_e32 v84, v84
	v_exp_f32_e32 v85, v85
	v_exp_f32_e32 v86, v86
	v_exp_f32_e32 v87, v87
	v_fma_f32 v88, v88, v250, v251
	v_fma_f32 v89, v89, v250, v251
	v_fma_f32 v90, v90, v250, v251
	v_fma_f32 v91, v91, v250, v251
	s_waitcnt lgkmcnt(8)
	v_mfma_f32_32x32x64_f8f6f4 v[18:33], v[108:115], v[124:131], v[18:33]
	v_add_f32_e32 v67, v84, v85
	v_add_f32_e32 v68, v86, v87
	v_exp_f32_e32 v88, v88
	v_exp_f32_e32 v89, v89
	v_exp_f32_e32 v90, v90
	v_exp_f32_e32 v91, v91
	v_add_f32_e32 v67, v67, v68
	v_cvt_pk_fp8_f32 v164, v84, v85
	v_cvt_pk_fp8_f32 v164, v86, v87 op_sel:[0,0,1]
	v_fma_f32 v92, v92, v250, v251
	v_fma_f32 v93, v93, v250, v251
	v_fma_f32 v94, v94, v250, v251
	v_fma_f32 v95, v95, v250, v251
	v_add_f32_e32 v68, v88, v89
	v_add_f32_e32 v69, v90, v91
	s_waitcnt lgkmcnt(6)
	v_mfma_f32_32x32x64_f8f6f4 v[50:65], v[108:115], v[202:209], v[50:65]
	ds_read_b128 v[202:205], v189 offset:32768
	ds_read_b128 v[206:209], v190 offset:32768
	v_exp_f32_e32 v92, v92
	v_exp_f32_e32 v93, v93
	v_exp_f32_e32 v94, v94
	v_exp_f32_e32 v95, v95
	v_add_f32_e32 v68, v68, v69
	v_cvt_pk_fp8_f32 v165, v88, v89
	v_cvt_pk_fp8_f32 v165, v90, v91 op_sel:[0,0,1]
	v_fma_f32 v96, v96, v250, v251
	v_fma_f32 v97, v97, v250, v251
	v_fma_f32 v98, v98, v250, v251
	v_fma_f32 v99, v99, v250, v251
	v_add_f32_e32 v67, v67, v68
	v_add_f32_e32 v68, v92, v93
	v_add_f32_e32 v69, v94, v95
	s_waitcnt lgkmcnt(6)
	v_mfma_f32_32x32x64_f8f6f4 v[34:49], v[108:115], v[210:217], v[34:49]
	ds_read_b128 v[210:213], v191 offset:32768
	ds_read_b128 v[214:217], v192 offset:32768
	v_exp_f32_e32 v96, v96
	v_exp_f32_e32 v97, v97
	v_exp_f32_e32 v98, v98
	v_exp_f32_e32 v99, v99
	v_add_f32_e32 v68, v68, v69
	v_cvt_pk_fp8_f32 v166, v92, v93
	v_cvt_pk_fp8_f32 v166, v94, v95 op_sel:[0,0,1]
	v_add_f32_e32 v67, v67, v68
	v_add_f32_e32 v68, v96, v97
	v_add_f32_e32 v69, v98, v99
	s_add_u32 s60, s60, 0x4000
	s_addc_u32 s61, s61, 0
	v_add_f32_e32 v68, v68, v69
	v_cvt_pk_fp8_f32 v167, v96, v97
	v_cvt_pk_fp8_f32 v167, v98, v99 op_sel:[0,0,1]
	v_add_f32_e32 v67, v67, v68
	ds_write_b128 v194, v[164:167]
	v_cmp_ge_f32_e64 s[52:53], s42, v67
	v_add_f32_e32 v66, v66, v67
	s_add_i32 s43, s43, 1
	s_nop 0
	s_and_b64 s[54:55], s[54:55], s[52:53]
	s_waitcnt lgkmcnt(7)
	v_mfma_i32_32x32x32_i8 v[84:99], v[218:221], v[132:135], v[226:241]
	v_mfma_i32_32x32x32_i8 v[84:99], v[222:225], v[136:139], v[84:99]
	s_waitcnt vmcnt(2) lgkmcnt(0)
	s_barrier
.Lat_u4:
	ds_read_b128 v[108:111], v193
	ds_read_b128 v[112:115], v193 offset:16
	v_mfma_i32_32x32x32_i8 v[84:99], v[242:245], v[140:143], v[84:99]
	ds_read_b128 v[116:119], v195 offset:22528
	ds_read_b128 v[120:123], v196 offset:22528
	s_add_i32 m0, s31, 65536
	ds_read_b128 v[124:127], v195 offset:20480
	global_load_lds_dwordx4 v252, s[60:61]
	s_add_i32 m0, s31, 73728
	v_mfma_i32_32x32x32_i8 v[84:99], v[246:249], v[144:147], v[84:99]
	global_load_lds_dwordx4 v254, s[60:61]
	ds_read_b128 v[128:131], v196 offset:20480
	v_mfma_i32_32x32x32_i8 v[84:99], v[202:205], v[148:151], v[84:99]
	ds_read_b128 v[202:205], v195 offset:16384
	v_mfma_i32_32x32x32_i8 v[84:99], v[206:209], v[152:155], v[84:99]
	ds_read_b128 v[206:209], v196 offset:16384
	v_mfma_i32_32x32x32_i8 v[84:99], v[210:213], v[156:159], v[84:99]
	ds_read_b128 v[210:213], v195 offset:18432
	v_mfma_i32_32x32x32_i8 v[84:99], v[214:217], v[160:163], v[84:99]
	ds_read_b128 v[214:217], v196 offset:18432
	v_readlane_b32 s50, v182, s43
	s_waitcnt lgkmcnt(6)
	v_mfma_f32_32x32x64_f8f6f4 v[2:17], v[108:115], v[116:123], v[2:17]
	ds_read_b128 v[218:221], v185
	ds_read_b128 v[222:225], v186
	ds_read_b128 v[242:245], v187
	ds_read_b128 v[246:249], v188
	v_mul_f32_e32 v82, s50, v168
	v_mul_f32_e32 v250, 0x3db8aa3b, v82
	v_fmamk_f32 v251, v250, 0xcb400000, v200
	s_mov_b32 m0, s31
	v_fma_f32 v84, v84, v250, v251
	global_load_lds_dwordx4 v255, s[60:61]
	s_add_i32 m0, s31, 8192
	v_fma_f32 v85, v85, v250, v251
	global_load_lds_dwordx4 v201, s[60:61]
	v_fma_f32 v86, v86, v250, v251
	v_fma_f32 v87, v87, v250, v251
	v_exp_f32_e32 v84, v84
	v_exp_f32_e32 v85, v85
	v_exp_f32_e32 v86, v86
	v_exp_f32_e32 v87, v87
	v_fma_f32 v88, v88, v250, v251
	v_fma_f32 v89, v89, v250, v251
	v_fma_f32 v90, v90, v250, v251
	v_fma_f32 v91, v91, v250, v251
	s_waitcnt lgkmcnt(8)
	v_mfma_f32_32x32x64_f8f6f4 v[18:33], v[108:115], v[124:131], v[18:33]
	v_add_f32_e32 v67, v84, v85
	v_add_f32_e32 v68, v86, v87
	v_exp_f32_e32 v88, v88
	v_exp_f32_e32 v89, v89
	v_exp_f32_e32 v90, v90
	v_exp_f32_e32 v91, v91
	v_add_f32_e32 v67, v67, v68
	v_cvt_pk_fp8_f32 v164, v84, v85
	v_cvt_pk_fp8_f32 v164, v86, v87 op_sel:[0,0,1]
	v_fma_f32 v92, v92, v250, v251
	v_fma_f32 v93, v93, v250, v251
	v_fma_f32 v94, v94, v250, v251
	v_fma_f32 v95, v95, v250, v251
	v_add_f32_e32 v68, v88, v89
	v_add_f32_e32 v69, v90, v91
	s_waitcnt lgkmcnt(6)
	v_mfma_f32_32x32x64_f8f6f4 v[50:65], v[108:115], v[202:209], v[50:65]
	ds_read_b128 v[202:205], v189
	ds_read_b128 v[206:209], v190
	v_exp_f32_e32 v92, v92
	v_exp_f32_e32 v93, v93
	v_exp_f32_e32 v94, v94
	v_exp_f32_e32 v95, v95
	v_add_f32_e32 v68, v68, v69
	v_cvt_pk_fp8_f32 v165, v88, v89
	v_cvt_pk_fp8_f32 v165, v90, v91 op_sel:[0,0,1]
	v_fma_f32 v96, v96, v250, v251
	v_fma_f32 v97, v97, v250, v251
	v_fma_f32 v98, v98, v250, v251
	v_fma_f32 v99, v99, v250, v251
	v_add_f32_e32 v67, v67, v68
	v_add_f32_e32 v68, v92, v93
	v_add_f32_e32 v69, v94, v95
	s_waitcnt lgkmcnt(6)
	v_mfma_f32_32x32x64_f8f6f4 v[34:49], v[108:115], v[210:217], v[34:49]
	ds_read_b128 v[210:213], v191
	ds_read_b128 v[214:217], v192
	v_exp_f32_e32 v96, v96
	v_exp_f32_e32 v97, v97
	v_exp_f32_e32 v98, v98
	v_exp_f32_e32 v99, v99
	v_add_f32_e32 v68, v68, v69
	v_cvt_pk_fp8_f32 v166, v92, v93
	v_cvt_pk_fp8_f32 v166, v94, v95 op_sel:[0,0,1]
	v_add_f32_e32 v67, v67, v68
	v_add_f32_e32 v68, v96, v97
	v_add_f32_e32 v69, v98, v99
	s_add_u32 s60, s60, 0x4000
	s_addc_u32 s61, s61, 0
	v_add_f32_e32 v68, v68, v69
	v_cvt_pk_fp8_f32 v167, v96, v97
	v_cvt_pk_fp8_f32 v167, v98, v99 op_sel:[0,0,1]
	v_add_f32_e32 v67, v67, v68
	ds_write_b128 v194, v[164:167] offset:8192
	v_cmp_ge_f32_e64 s[52:53], s42, v67
	v_add_f32_e32 v66, v66, v67
	s_add_i32 s43, s43, 1
	s_nop 0
	s_and_b64 s[54:55], s[54:55], s[52:53]
	s_waitcnt lgkmcnt(7)
	v_mfma_i32_32x32x32_i8 v[84:99], v[218:221], v[132:135], v[226:241]
	v_mfma_i32_32x32x32_i8 v[84:99], v[222:225], v[136:139], v[84:99]
	s_waitcnt vmcnt(2) lgkmcnt(0)
	s_barrier

.Lat_k5:
	ds_read_b128 v[128:131], v196 offset:36864
	v_mfma_i32_32x32x32_i8 v[84:99], v[202:205], v[148:151], v[84:99]
	ds_read_b128 v[202:205], v195 offset:32768
	v_mfma_i32_32x32x32_i8 v[84:99], v[206:209], v[152:155], v[84:99]
	ds_read_b128 v[206:209], v196 offset:32768
	v_mfma_i32_32x32x32_i8 v[84:99], v[210:213], v[156:159], v[84:99]
	ds_read_b128 v[210:213], v195 offset:34816
	v_mfma_i32_32x32x32_i8 v[84:99], v[214:217], v[160:163], v[84:99]
	ds_read_b128 v[214:217], v196 offset:34816
	v_readlane_b32 s50, v182, s43
	s_waitcnt lgkmcnt(6)
	v_mfma_f32_32x32x64_f8f6f4 v[2:17], v[108:115], v[116:123], v[2:17]
	ds_read_b128 v[218:221], v185 offset:16384
	ds_read_b128 v[222:225], v186 offset:16384
	ds_read_b128 v[242:245], v187 offset:16384
	ds_read_b128 v[246:249], v188 offset:16384
	v_mul_f32_e32 v82, s50, v168
	v_mul_f32_e32 v250, 0x3db8aa3b, v82
	v_fmamk_f32 v251, v250, 0xcb400000, v200
	s_add_i32 m0, s31, 16384
	v_fma_f32 v84, v84, v250, v251
	global_load_lds_dwordx4 v255, s[60:61]
	s_add_i32 m0, s31, 24576
	v_fma_f32 v85, v85, v250, v251
	global_load_lds_dwordx4 v201, s[60:61]
	v_fma_f32 v86, v86, v250, v251
	v_fma_f32 v87, v87, v250, v251
	v_exp_f32_e32 v84, v84
	v_exp_f32_e32 v85, v85
	v_exp_f32_e32 v86, v86
	v_exp_f32_e32 v87, v87
	v_fma_f32 v88, v88, v250, v251
	v_fma_f32 v89, v89, v250, v251
	v_fma_f32 v90, v90, v250, v251
	v_fma_f32 v91, v91, v250, v251
	s_waitcnt lgkmcnt(8)
	v_mfma_f32_32x32x64_f8f6f4 v[18:33], v[108:115], v[124:131], v[18:33]
	v_add_f32_e32 v67, v84, v85
	v_add_f32_e32 v68, v86, v87
	v_exp_f32_e32 v88, v88
	v_exp_f32_e32 v89, v89
	v_exp_f32_e32 v90, v90
	v_exp_f32_e32 v91, v91
	v_add_f32_e32 v67, v67, v68
	v_cvt_pk_fp8_f32 v164, v84, v85
	v_cvt_pk_fp8_f32 v164, v86, v87 op_sel:[0,0,1]
	v_fma_f32 v92, v92, v250, v251
	v_fma_f32 v93, v93, v250, v251
	v_fma_f32 v94, v94, v250, v251
	v_fma_f32 v95, v95, v250, v251
	v_add_f32_e32 v68, v88, v89
	v_add_f32_e32 v69, v90, v91
	s_waitcnt lgkmcnt(6)
	v_mfma_f32_32x32x64_f8f6f4 v[50:65], v[108:115], v[202:209], v[50:65]
	ds_read_b128 v[202:205], v189 offset:16384
	ds_read_b128 v[206:209], v190 offset:16384
	v_exp_f32_e32 v92, v92
	v_exp_f32_e32 v93, v93
	v_exp_f32_e32 v94, v94
	v_exp_f32_e32 v95, v95
	v_add_f32_e32 v68, v68, v69
	v_cvt_pk_fp8_f32 v165, v88, v89
	v_cvt_pk_fp8_f32 v165, v90, v91 op_sel:[0,0,1]
	v_fma_f32 v96, v96, v250, v251
	v_fma_f32 v97, v97, v250, v251
	v_fma_f32 v98, v98, v250, v251
	v_fma_f32 v99, v99, v250, v251
	v_add_f32_e32 v67, v67, v68
	v_add_f32_e32 v68, v92, v93
	v_add_f32_e32 v69, v94, v95
	s_waitcnt lgkmcnt(6)
	v_mfma_f32_32x32x64_f8f6f4 v[34:49], v[108:115], v[210:217], v[34:49]
	ds_read_b128 v[210:213], v191 offset:16384
	ds_read_b128 v[214:217], v192 offset:16384
	v_exp_f32_e32 v96, v96
	v_exp_f32_e32 v97, v97
	v_exp_f32_e32 v98, v98
	v_exp_f32_e32 v99, v99
	v_add_f32_e32 v68, v68, v69
	v_cvt_pk_fp8_f32 v166, v92, v93
	v_cvt_pk_fp8_f32 v166, v94, v95 op_sel:[0,0,1]
	v_add_f32_e32 v67, v67, v68
	v_add_f32_e32 v68, v96, v97
	v_add_f32_e32 v69, v98, v99
	s_add_u32 s60, s60, 0x4000
	s_addc_u32 s61, s61, 0
	v_add_f32_e32 v68, v68, v69
	v_cvt_pk_fp8_f32 v167, v96, v97
	v_cvt_pk_fp8_f32 v167, v98, v99 op_sel:[0,0,1]
	v_add_f32_e32 v67, v67, v68
	ds_write_b128 v194, v[164:167]
	v_cmp_ge_f32_e64 s[52:53], s42, v67
	v_add_f32_e32 v66, v66, v67
	s_add_i32 s43, s43, 1
	s_nop 0
	s_and_b64 s[54:55], s[54:55], s[52:53]
	s_waitcnt lgkmcnt(7)
	v_mfma_i32_32x32x32_i8 v[84:99], v[218:221], v[132:135], v[226:241]
	v_mfma_i32_32x32x32_i8 v[84:99], v[222:225], v[136:139], v[84:99]
	s_cmp_gt_u32 s43, 30
	s_cbranch_scc1 .Lat_drain
	s_waitcnt vmcnt(2) lgkmcnt(0)
	s_barrier
	s_branch .Lat_u0

.LBB2_16:
	v_add_u32_e32 v110, 0, v195
	v_add_u32_e32 v118, 0, v196
	ds_read_b128 v[82:85], v193 offset:8192
	ds_read_b128 v[86:89], v193 offset:8208
	ds_read_b128 v[90:93], v110 offset:16384
	ds_read_b128 v[98:101], v110 offset:18432
	ds_read_b128 v[94:97], v118 offset:16384
	ds_read_b128 v[102:105], v118 offset:18432
	ds_read_b128 v[106:109], v110 offset:20480
	ds_read_b128 v[114:117], v110 offset:22528
	ds_read_b128 v[110:113], v118 offset:20480
	ds_read_b128 v[118:121], v118 offset:22528
	s_waitcnt lgkmcnt(0)
	v_mfma_f32_32x32x64_f8f6f4 v[50:65], v[82:89], v[90:97], v[50:65]
	s_cmp_lg_u32 s39, 0
	s_cselect_b64 s[0:1], -1, 0
	v_cmp_eq_u32_e32 vcc, 0, v198
	s_and_b64 s[6:7], vcc, s[0:1]
	v_mfma_f32_32x32x64_f8f6f4 v[34:49], v[82:89], v[98:105], v[34:49]
	v_mfma_f32_32x32x64_f8f6f4 v[18:33], v[82:89], v[106:113], v[18:33]
	v_mfma_f32_32x32x64_f8f6f4 v[2:17], v[82:89], v[114:121], v[2:17]
	s_and_saveexec_b64 s[0:1], s[6:7]
	s_add_i32 s6, 0, 0x1cc00
	v_mov_b32_e32 v82, 1
	v_mov_b32_e32 v83, s6
	ds_write_b32 v83, v82
	s_or_b64 exec, exec, s[0:1]
	s_add_i32 s0, 0, 0x1cc00
	v_mov_b32_e32 v82, s0
	s_waitcnt vmcnt(0) lgkmcnt(0)
	s_barrier
	ds_read_b32 v82, v82
	s_waitcnt lgkmcnt(0)
	v_cmp_eq_u32_e32 vcc, 0, v82
	s_cbranch_vccnz .Lat_lsum
	s_mov_b32 m0, s36
	s_barrier
	global_load_lds_dwordx4 v[174:175], off
	s_mov_b32 m0, s35
	s_lshl_b32 s0, s34, 5
	global_load_lds_dwordx4 v[176:177], off
	s_mov_b32 m0, s31
	s_lshl_b32 s1, s34, 7
	global_load_lds_dwordx4 v[178:179], off
	s_mov_b32 m0, s37
	s_add_i32 s1, s1, 0
	global_load_lds_dwordx4 v[180:181], off
	v_or_b32_e32 v2, s0, v1
	s_add_i32 s1, s1, 0x1c400
	v_bitop3_b32 v4, s0, 32, v1 bitop3:0x36
	v_lshlrev_b32_e32 v2, 2, v2
	v_add_u32_e32 v3, s1, v199
	v_lshlrev_b32_e32 v5, 4, v183
	v_lshlrev_b32_e32 v4, 2, v4
	v_add3_u32 v120, s38, v2, v199
	v_mov_b32_e32 v2, 0
	s_mov_b32 s20, 0
	v_lshl_add_u32 v118, v1, 2, v3
	v_add3_u32 v119, s38, v4, v199
	v_mov_b32_e32 v101, 0xf149f2ca
	s_mov_b64 s[0:1], 0
	s_mov_b64 s[6:7], 0x4000
	s_mov_b64 s[8:9], 0x6000
	v_add_u32_e32 v121, v3, v5
	s_mov_b32 s21, 0xbdb8aa3b
	v_mov_b32_e32 v82, 0x4b400000
	v_mov_b32_e32 v100, 0x38383838
	v_mov_b32_e32 v3, v2
	v_mov_b32_e32 v4, v2
	v_mov_b32_e32 v5, v2
	v_mov_b32_e32 v6, v2
	v_mov_b32_e32 v7, v2
	v_mov_b32_e32 v8, v2
	v_mov_b32_e32 v9, v2
	v_mov_b32_e32 v10, v2
	v_mov_b32_e32 v11, v2
	v_mov_b32_e32 v12, v2
	v_mov_b32_e32 v13, v2
	v_mov_b32_e32 v14, v2
	v_mov_b32_e32 v15, v2
	v_mov_b32_e32 v16, v2
	v_mov_b32_e32 v17, v2
	v_mov_b32_e32 v18, v2
	v_mov_b32_e32 v19, v2
	v_mov_b32_e32 v20, v2
	v_mov_b32_e32 v21, v2
	v_mov_b32_e32 v22, v2
	v_mov_b32_e32 v23, v2
	v_mov_b32_e32 v24, v2
	v_mov_b32_e32 v25, v2
	v_mov_b32_e32 v26, v2
	v_mov_b32_e32 v27, v2
	v_mov_b32_e32 v28, v2
	v_mov_b32_e32 v29, v2
	v_mov_b32_e32 v30, v2
	v_mov_b32_e32 v31, v2
	v_mov_b32_e32 v32, v2
	v_mov_b32_e32 v33, v2
	v_mov_b32_e32 v34, v2
	v_mov_b32_e32 v35, v2
	v_mov_b32_e32 v36, v2
	v_mov_b32_e32 v37, v2
	v_mov_b32_e32 v38, v2
	v_mov_b32_e32 v39, v2
	v_mov_b32_e32 v40, v2
	v_mov_b32_e32 v41, v2
	v_mov_b32_e32 v42, v2
	v_mov_b32_e32 v43, v2
	v_mov_b32_e32 v44, v2
	v_mov_b32_e32 v45, v2
	v_mov_b32_e32 v46, v2
	v_mov_b32_e32 v47, v2
	v_mov_b32_e32 v48, v2
	v_mov_b32_e32 v49, v2
	v_mov_b32_e32 v50, v2
	v_mov_b32_e32 v51, v2
	v_mov_b32_e32 v52, v2
	v_mov_b32_e32 v53, v2
	v_mov_b32_e32 v54, v2
	v_mov_b32_e32 v55, v2
	v_mov_b32_e32 v56, v2
	v_mov_b32_e32 v57, v2
	v_mov_b32_e32 v58, v2
	v_mov_b32_e32 v59, v2
	v_mov_b32_e32 v60, v2
	v_mov_b32_e32 v61, v2
	v_mov_b32_e32 v62, v2
	v_mov_b32_e32 v63, v2
	v_mov_b32_e32 v64, v2
	v_mov_b32_e32 v65, v2
	v_mov_b32_e32 v66, v2
	v_mov_b32_e32 v67, v2
	v_mov_b32_e32 v68, v2
	v_mov_b32_e32 v69, v2
	v_mov_b32_e32 v70, v2
	v_mov_b32_e32 v71, v2
	v_mov_b32_e32 v72, v2
	v_mov_b32_e32 v73, v2
	v_mov_b32_e32 v74, v2
	v_mov_b32_e32 v75, v2
	v_mov_b32_e32 v76, v2
	v_mov_b32_e32 v77, v2
	v_mov_b32_e32 v78, v2
	v_mov_b32_e32 v79, v2
	v_mov_b32_e32 v80, v2
	v_mov_b32_e32 v81, v2
	s_waitcnt vmcnt(0) lgkmcnt(0)
	s_barrier
	s_cmp_eq_u32 s0, 0x7c000
	s_movk_i32 s22, 0x4000
	s_cbranch_scc1 .LBB2_21

.Lat_lsum:
	v_mov_b32_e32 v67, v66
	s_lshl_b32 s0, s34, 9
	s_lshl_b32 s1, s33, 2
	s_add_i32 s0, s0, 0x1c000
	v_permlane32_swap_b32_e32 v67, v66
	s_add_i32 s0, s0, s1
	v_lshl_add_u32 v68, v1, 2, s0
	v_add_f32_e32 v66, v66, v67
	ds_write_b32 v68, v66
	s_add_i32 s1, s1, 0x1c000
	v_lshl_add_u32 v69, v183, 4, s1
	s_waitcnt lgkmcnt(0)
	s_barrier
	ds_read_b128 v[70:73], v69
	ds_read_b128 v[74:77], v69 offset:32
	ds_read_b128 v[78:81], v69 offset:64
	ds_read_b128 v[82:85], v69 offset:96
	ds_read_b128 v[86:89], v69 offset:512
	ds_read_b128 v[90:93], v69 offset:544
	ds_read_b128 v[94:97], v69 offset:576
	ds_read_b128 v[98:101], v69 offset:608
	s_waitcnt lgkmcnt(0)
	v_add_f32_e32 v66, v70, v86
	v_add_f32_e32 v67, v71, v87
	v_add_f32_e32 v68, v72, v88
	v_add_f32_e32 v69, v73, v89
	v_add_f32_e32 v70, v74, v90
	v_add_f32_e32 v71, v75, v91
	v_add_f32_e32 v72, v76, v92
	v_add_f32_e32 v73, v77, v93
	v_add_f32_e32 v74, v78, v94
	v_add_f32_e32 v75, v79, v95
	v_add_f32_e32 v76, v80, v96
	v_add_f32_e32 v77, v81, v97
	v_add_f32_e32 v78, v82, v98
	v_add_f32_e32 v79, v83, v99
	v_add_f32_e32 v80, v84, v100
	v_add_f32_e32 v81, v85, v101
